# s17 + PROJ last-unit write-through only for the column tiles the x1 pre-pass does not read (pn >= 20)
# baseline (speedup 1.0000x reference)
; __device__ __forceinline__ unsigned cvt_pk_f16(float lo, float hi) { f32x2 v = {lo, hi}; h16x2 b = __builtin_convertvector(v, h16x2); return __builtin_bit_cast(unsigned, b); }
; #define PG8_BAR __builtin_amdgcn_s_barrier()
; #define PG8_BAR __builtin_amdgcn_s_barrier()
;     __device__ __forceinline__ void operator()(const f32x4 (&acc)[2][2][4][2], const Unit& u, int wr, int wc, int fr, int fq) const {
;         const int row0 = u.pm * BM + wr * 64 + fr, col0 = u.pn * BM + wc * 32 + 8 * fq;
; #pragma unroll
;         for (int ai = 0; ai < 2; ++ai)
; #pragma unroll
;             for (int m = 0; m < 4; ++m) { h16* rowp = C + (size_t)(row0 + ai * HALF + m * 16) * ldc + col0;
; #pragma unroll
;                 for (int bj = 0; bj < 2; ++bj) { const f32x4 v0 = acc[ai][bj][m][0], v1 = acc[ai][bj][m][1];
;                     u32x4 w; w.x = cvt_pk_f16(v0[0], v0[1]); w.y = cvt_pk_f16(v0[2], v0[3]); w.z = cvt_pk_f16(v1[0], v1[1]); w.w = cvt_pk_f16(v1[2], v1[3]);
;                     *(u32x4*)(rowp + bj * HALF) = w; } }
;     }
; template <class Epi, class Sched, bool ALIGN_EPI = true>
; __device__ __forceinline__ void gemm_phase(PG8_LAS unsigned char* lds, const Gemm g, const Sched& S, const Epi& E) {
;     ...
;         if constexpr (ALIGN_EPI) { if (wr == 0) PG8_BAR; }
;         if constexpr (!Epi::AFTER_DRAIN) E(acc, cur, wr, wc, fr, fq);
;         if (!has_next) break;
.LBB0_983:
	s_cmp_lt_u32 s34, 20
	s_cbranch_scc1 .Lproj_epi_plain
	s_and_b64 vcc, exec, s[38:39]
	s_cbranch_vccz .Lproj_epi_last
